# v22 + P9 counted-wait split: K/V band waited at item end (vmcnt 6), Q waited at the next item top (vmcnt 2)
# speedup vs baseline: 1.0048x; 1.0018x over previous
.LBB0_869:
	s_ashr_i32 s38, s37, 31
	s_lshr_b32 s2, s38, 25
	s_add_i32 s2, s37, s2
	s_ashr_i32 s39, s2, 7
	s_lshr_b32 s2, s39, 30
	s_add_i32 s2, s39, s2
	s_and_b32 s2, s2, 0x3ffffffc
	s_sub_i32 s2, s39, s2
	s_lshl_b32 s2, s2, 2
	s_or_b32 s8, s2, s22
	s_mul_i32 s2, s34, 0xd000
	s_ashr_i32 s9, s8, 31
	s_add_i32 s36, s2, 0
	s_add_i32 s35, s37, s72
	s_add_i32 s2, s8, 16
	s_nop 3
	v_readlane_b32 s3, v255, s2
	s_nop 1
	v_mov_b32_e32 v156, s3
	s_waitcnt vmcnt(2)
	s_cmpk_gt_i32 s35, 0xfff
	s_cbranch_scc1 .Lp9_kvdone
	s_ashr_i32 s2, s35, 31
	s_lshr_b32 s3, s2, 23
	s_lshr_b32 s2, s2, 25
	s_add_i32 s2, s35, s2
	s_ashr_i32 s6, s2, 7
	s_add_i32 s3, s35, s3
	s_lshr_b32 s2, s6, 30
	s_ashr_i32 s14, s3, 9
	s_add_i32 s2, s6, s2
	s_lshl_b32 s9, s6, 13
	s_and_b32 s2, s2, -4
	s_ashr_i32 s15, s14, 31
	s_sub_i32 s16, s6, s2
	s_lshl_b64 s[2:3], s[14:15], 22
	s_add_u32 s40, s18, s2
	s_addc_u32 s41, s19, s3
	s_lshl_b32 s16, s16, 6
	s_ashr_i32 s17, s16, 31
	s_lshl_b64 s[2:3], s[16:17], 1
	s_add_u32 s2, s40, s2
	s_addc_u32 s3, s41, s3
	v_mov_b32_e32 v137, v112
	v_lshl_add_u64 v[118:119], s[2:3], 0, v[136:137]
	s_sub_i32 s2, s30, s9
	v_mov_b32_e32 v113, v112
	v_add_u32_e32 v84, s2, v152
	v_mov_b32_e32 v114, v112
	v_mov_b32_e32 v115, v112
	v_mov_b64_e32 v[80:81], v[112:113]
	v_cmp_lt_i32_e32 vcc, -1, v84
	v_mov_b64_e32 v[82:83], v[114:115]
	s_and_saveexec_b64 s[2:3], vcc
	s_cbranch_execz .LBB0_872
	v_mov_b32_e32 v85, v112
	v_lshlrev_b64 v[80:81], 9, v[84:85]
	v_lshl_add_u64 v[80:81], v[118:119], 0, v[80:81]
	global_load_dwordx4 v[80:83], v[80:81], off

.LBB0_885:
	s_lshl_b32 s2, s39, 13
	s_sub_i32 s14, s27, s2
	s_add_i32 s6, s29, s2
	s_lshr_b32 s2, s38, 23
	s_add_i32 s2, s37, s2
	s_ashr_i32 s16, s2, 9
	v_cmp_gt_i32_e64 s[2:3], 1, v157
	s_ashr_i32 s17, s16, 31
	s_cmpk_lt_i32 s14, 0x80
	v_cndmask_b32_e64 v1, v155, v1, s[2:3]
	v_cmp_gt_i32_e64 s[2:3], 2, v157
	v_cmp_gt_i32_e32 vcc, 0, v157
	v_mul_f32_e32 v113, 0x3fb8aa3b, v156
	v_cndmask_b32_e64 v2, v155, v2, s[2:3]
	v_cmp_gt_i32_e64 s[2:3], 3, v157
	v_cndmask_b32_e32 v0, v155, v0, vcc
	s_cselect_b64 vcc, -1, 0
	v_cndmask_b32_e64 v3, v155, v3, s[2:3]
	v_cmp_gt_i32_e64 s[2:3], 8, v157
	v_cndmask_b32_e32 v0, v0, v155, vcc
	v_cndmask_b32_e32 v1, v1, v155, vcc
	v_cndmask_b32_e64 v4, v155, v4, s[2:3]
	v_cmp_gt_i32_e64 s[2:3], 9, v157
	v_max3_f32 v113, v113, v0, v1
	v_cndmask_b32_e32 v2, v2, v155, vcc
	v_cndmask_b32_e64 v5, v155, v5, s[2:3]
	v_cmp_gt_i32_e64 s[2:3], 10, v157
	v_cndmask_b32_e32 v3, v3, v155, vcc
	v_max3_f32 v113, v113, v2, v3
	v_cndmask_b32_e64 v6, v155, v6, s[2:3]
	v_cmp_gt_i32_e64 s[2:3], 11, v157
	v_cndmask_b32_e32 v4, v4, v155, vcc
	v_cndmask_b32_e32 v5, v5, v155, vcc
	v_cndmask_b32_e64 v7, v155, v7, s[2:3]
	v_cmp_gt_i32_e64 s[2:3], 16, v157
	v_max3_f32 v113, v113, v4, v5
	v_cndmask_b32_e32 v6, v6, v155, vcc
	v_cndmask_b32_e64 v8, v155, v8, s[2:3]
	v_cmp_gt_i32_e64 s[2:3], 17, v157
	v_cndmask_b32_e32 v7, v7, v155, vcc
	v_max3_f32 v113, v113, v6, v7
	v_cndmask_b32_e64 v9, v155, v9, s[2:3]
	v_cmp_gt_i32_e64 s[2:3], 18, v157
	v_cndmask_b32_e32 v8, v8, v155, vcc
	v_cndmask_b32_e32 v9, v9, v155, vcc
	v_cndmask_b32_e64 v10, v155, v10, s[2:3]
	v_cmp_gt_i32_e64 s[2:3], 19, v157
	v_max3_f32 v113, v113, v8, v9
	v_cndmask_b32_e32 v10, v10, v155, vcc
	v_cndmask_b32_e64 v11, v155, v11, s[2:3]
	v_cmp_gt_i32_e64 s[2:3], 24, v157
	v_cndmask_b32_e32 v11, v11, v155, vcc
	s_cmp_gt_u32 s6, 32
	v_cndmask_b32_e64 v12, v155, v12, s[2:3]
	v_cmp_gt_i32_e64 s[2:3], 25, v157
	v_max3_f32 v113, v113, v10, v11
	v_cndmask_b32_e32 v12, v12, v155, vcc
	v_cndmask_b32_e64 v13, v155, v13, s[2:3]
	v_cmp_gt_i32_e64 s[2:3], 26, v157
	v_cndmask_b32_e32 v13, v13, v155, vcc
	v_max3_f32 v113, v113, v12, v13
	v_cndmask_b32_e64 v14, v155, v14, s[2:3]
	v_cmp_gt_i32_e64 s[2:3], 27, v157
	v_cndmask_b32_e32 v14, v14, v155, vcc
	s_nop 0
	v_cndmask_b32_e64 v15, v155, v15, s[2:3]
	s_cselect_b64 s[2:3], -1, 0
	v_cndmask_b32_e32 v15, v15, v155, vcc
	s_and_b64 s[2:3], vcc, s[2:3]
	v_max3_f32 v113, v113, v14, v15
	v_cndmask_b32_e64 v16, v16, v155, s[2:3]
	v_cndmask_b32_e64 v17, v17, v155, s[2:3]
	v_max3_f32 v113, v113, v16, v17
	v_cndmask_b32_e64 v18, v18, v155, s[2:3]
	v_cndmask_b32_e64 v19, v19, v155, s[2:3]
	v_max3_f32 v113, v113, v18, v19
	v_cndmask_b32_e64 v20, v20, v155, s[2:3]
	v_cndmask_b32_e64 v21, v21, v155, s[2:3]
	v_max3_f32 v113, v113, v20, v21
	v_cndmask_b32_e64 v22, v22, v155, s[2:3]
	v_cndmask_b32_e64 v23, v23, v155, s[2:3]
	v_max3_f32 v113, v113, v22, v23
	v_cndmask_b32_e64 v24, v24, v155, s[2:3]
	v_cndmask_b32_e64 v25, v25, v155, s[2:3]
	v_max3_f32 v113, v113, v24, v25
	v_cndmask_b32_e64 v26, v26, v155, s[2:3]
	v_cndmask_b32_e64 v27, v27, v155, s[2:3]
	s_cmp_gt_u32 s6, 64
	v_max3_f32 v113, v113, v26, v27
	v_cndmask_b32_e64 v28, v28, v155, s[2:3]
	v_cndmask_b32_e64 v29, v29, v155, s[2:3]
	v_cndmask_b32_e64 v30, v30, v155, s[2:3]
	v_cndmask_b32_e64 v31, v31, v155, s[2:3]
	s_cselect_b64 s[2:3], -1, 0
	v_max3_f32 v113, v113, v28, v29
	s_and_b64 s[2:3], vcc, s[2:3]
	v_max3_f32 v113, v113, v30, v31
	v_cndmask_b32_e64 v135, v32, v155, s[2:3]
	v_cndmask_b32_e64 v137, v33, v155, s[2:3]
	v_max3_f32 v32, v113, v135, v137
	v_cndmask_b32_e64 v113, v34, v155, s[2:3]
	v_cndmask_b32_e64 v138, v35, v155, s[2:3]
	v_max3_f32 v32, v32, v113, v138
	v_cndmask_b32_e64 v139, v36, v155, s[2:3]
	v_cndmask_b32_e64 v158, v37, v155, s[2:3]
	v_max3_f32 v32, v32, v139, v158
	v_cndmask_b32_e64 v159, v38, v155, s[2:3]
	v_cndmask_b32_e64 v160, v39, v155, s[2:3]
	s_cmpk_gt_u32 s6, 0x60
	v_max3_f32 v32, v32, v159, v160
	v_cndmask_b32_e64 v161, v40, v155, s[2:3]
	v_cndmask_b32_e64 v162, v41, v155, s[2:3]
	v_cndmask_b32_e64 v163, v42, v155, s[2:3]
	v_cndmask_b32_e64 v164, v43, v155, s[2:3]
	v_cndmask_b32_e64 v165, v44, v155, s[2:3]
	v_cndmask_b32_e64 v166, v45, v155, s[2:3]
	v_cndmask_b32_e64 v167, v46, v155, s[2:3]
	v_cndmask_b32_e64 v168, v47, v155, s[2:3]
	s_cselect_b64 s[2:3], -1, 0
	v_max3_f32 v32, v32, v161, v162
	s_and_b64 vcc, vcc, s[2:3]
	v_max3_f32 v32, v32, v163, v164
	v_cndmask_b32_e32 v169, v48, v155, vcc
	v_cndmask_b32_e32 v170, v49, v155, vcc
	v_cndmask_b32_e32 v171, v50, v155, vcc
	v_cndmask_b32_e32 v172, v51, v155, vcc
	v_cndmask_b32_e32 v52, v52, v155, vcc
	v_cndmask_b32_e32 v53, v53, v155, vcc
	v_cndmask_b32_e32 v54, v54, v155, vcc
	v_cndmask_b32_e32 v55, v55, v155, vcc
	v_cndmask_b32_e32 v56, v56, v155, vcc
	v_cndmask_b32_e32 v173, v57, v155, vcc
	v_cndmask_b32_e32 v174, v58, v155, vcc
	v_cndmask_b32_e32 v175, v59, v155, vcc
	v_cndmask_b32_e32 v176, v60, v155, vcc
	v_cndmask_b32_e32 v51, v61, v155, vcc
	v_cndmask_b32_e32 v50, v62, v155, vcc
	v_cndmask_b32_e32 v48, v63, v155, vcc
	s_cmp_lt_i32 s14, 0
	v_cmp_lt_i32_e32 vcc, -1, v157
	v_max3_f32 v32, v32, v165, v166
	v_cmp_lt_i32_e64 s[2:3], 0, v157
	v_cndmask_b32_e32 v33, v155, v64, vcc
	s_cselect_b64 vcc, -1, 0
	v_max3_f32 v32, v32, v167, v168
	v_cndmask_b32_e32 v49, v33, v155, vcc
	v_cndmask_b32_e64 v33, v155, v65, s[2:3]
	v_cmp_lt_i32_e64 s[2:3], 1, v157
	v_max3_f32 v32, v32, v169, v170
	v_cndmask_b32_e32 v45, v33, v155, vcc
	v_cndmask_b32_e64 v33, v155, v66, s[2:3]
	v_cmp_lt_i32_e64 s[2:3], 2, v157
	v_max3_f32 v32, v32, v171, v172
	v_cndmask_b32_e32 v46, v33, v155, vcc
	v_cndmask_b32_e64 v33, v155, v67, s[2:3]
	v_cmp_lt_i32_e64 s[2:3], 7, v157
	v_max3_f32 v32, v32, v52, v53
	v_cndmask_b32_e32 v47, v33, v155, vcc
	v_cndmask_b32_e64 v33, v155, v68, s[2:3]
	v_cmp_lt_i32_e64 s[2:3], 8, v157
	v_max3_f32 v32, v32, v54, v55
	v_cndmask_b32_e32 v44, v33, v155, vcc
	v_cndmask_b32_e64 v33, v155, v69, s[2:3]
	v_cmp_lt_i32_e64 s[2:3], 9, v157
	v_max3_f32 v32, v32, v56, v173
	v_cndmask_b32_e32 v43, v33, v155, vcc
	v_cndmask_b32_e64 v33, v155, v70, s[2:3]
	v_cmp_lt_i32_e64 s[2:3], 10, v157
	v_max3_f32 v32, v32, v174, v175
	v_cndmask_b32_e32 v42, v33, v155, vcc
	v_cndmask_b32_e64 v33, v155, v71, s[2:3]
	v_cmp_lt_i32_e64 s[2:3], 15, v157
	v_max3_f32 v32, v32, v176, v51
	v_cndmask_b32_e32 v40, v33, v155, vcc
	v_cndmask_b32_e64 v33, v155, v72, s[2:3]
	v_cmp_lt_i32_e64 s[2:3], 16, v157
	v_max3_f32 v32, v32, v50, v48
	v_cndmask_b32_e32 v41, v33, v155, vcc
	v_cndmask_b32_e64 v33, v155, v73, s[2:3]
	v_cmp_lt_i32_e64 s[2:3], 17, v157
	v_max3_f32 v32, v32, v49, v45
	v_cndmask_b32_e32 v39, v33, v155, vcc
	v_cndmask_b32_e64 v33, v155, v74, s[2:3]
	v_cmp_lt_i32_e64 s[2:3], 18, v157
	v_max3_f32 v32, v32, v46, v47
	v_cndmask_b32_e32 v38, v33, v155, vcc
	v_cndmask_b32_e64 v33, v155, v75, s[2:3]
	v_cmp_lt_i32_e64 s[2:3], 23, v157
	v_max3_f32 v32, v32, v44, v43
	v_cndmask_b32_e32 v37, v33, v155, vcc
	v_cndmask_b32_e64 v33, v155, v76, s[2:3]
	v_cmp_lt_i32_e64 s[2:3], 24, v157
	v_max3_f32 v32, v32, v42, v40
	v_cndmask_b32_e32 v34, v33, v155, vcc
	v_cndmask_b32_e64 v33, v155, v77, s[2:3]
	v_cmp_lt_i32_e64 s[2:3], 25, v157
	v_max3_f32 v32, v32, v41, v39
	v_cndmask_b32_e32 v35, v33, v155, vcc
	v_cndmask_b32_e64 v33, v155, v78, s[2:3]
	v_cmp_lt_i32_e64 s[2:3], 26, v157
	v_max3_f32 v32, v32, v38, v37
	v_cndmask_b32_e32 v36, v33, v155, vcc
	v_cndmask_b32_e64 v33, v155, v79, s[2:3]
	v_max3_f32 v32, v32, v34, v35
	v_cndmask_b32_e32 v33, v33, v155, vcc
	v_max3_f32 v32, v32, v36, v33
	ds_bpermute_b32 v57, v141, v32
	s_ashr_i32 s15, s14, 31
	s_lshl_b64 s[2:3], s[16:17], 23
	s_lshl_b64 s[14:15], s[14:15], 10
	s_add_u32 s2, s20, s2
	s_waitcnt lgkmcnt(0)
	v_max_f32_e32 v57, v57, v57
	v_max_f32_e32 v32, v32, v57
	v_sub_f32_e32 v0, v0, v32
	v_exp_f32_e32 v0, v0
	v_sub_f32_e32 v1, v1, v32
	v_exp_f32_e32 v1, v1
	v_sub_f32_e32 v2, v2, v32
	v_exp_f32_e32 v2, v2
	v_sub_f32_e32 v3, v3, v32
	v_exp_f32_e32 v3, v3
	v_sub_f32_e32 v4, v4, v32
	v_add_f32_e32 v57, 0, v0
	v_exp_f32_e32 v4, v4
	v_sub_f32_e32 v5, v5, v32
	v_add_f32_e32 v57, v1, v57
	v_exp_f32_e32 v5, v5
	v_sub_f32_e32 v6, v6, v32
	v_add_f32_e32 v57, v2, v57
	v_exp_f32_e32 v6, v6
	v_sub_f32_e32 v7, v7, v32
	v_add_f32_e32 v57, v3, v57
	v_exp_f32_e32 v7, v7
	v_sub_f32_e32 v8, v8, v32
	v_add_f32_e32 v57, v4, v57
	v_exp_f32_e32 v58, v8
	v_sub_f32_e32 v9, v9, v32
	v_add_f32_e32 v8, v5, v57
	v_exp_f32_e32 v57, v9
	v_sub_f32_e32 v9, v10, v32
	v_add_f32_e32 v8, v6, v8
	v_exp_f32_e32 v59, v9
	v_sub_f32_e32 v9, v11, v32
	v_add_f32_e32 v8, v7, v8
	v_exp_f32_e32 v60, v9
	v_sub_f32_e32 v9, v12, v32
	v_add_f32_e32 v8, v58, v8
	v_exp_f32_e32 v12, v9
	v_sub_f32_e32 v9, v13, v32
	v_add_f32_e32 v8, v57, v8
	v_exp_f32_e32 v13, v9
	v_sub_f32_e32 v9, v14, v32
	v_add_f32_e32 v8, v59, v8
	v_exp_f32_e32 v14, v9
	v_sub_f32_e32 v9, v15, v32
	v_add_f32_e32 v8, v60, v8
	v_exp_f32_e32 v15, v9
	v_sub_f32_e32 v9, v16, v32
	v_add_f32_e32 v8, v12, v8
	v_exp_f32_e32 v64, v9
	v_sub_f32_e32 v9, v17, v32
	v_add_f32_e32 v8, v13, v8
	v_exp_f32_e32 v65, v9
	v_sub_f32_e32 v9, v18, v32
	v_add_f32_e32 v8, v14, v8
	v_exp_f32_e32 v66, v9
	v_sub_f32_e32 v9, v19, v32
	v_add_f32_e32 v8, v15, v8
	v_exp_f32_e32 v67, v9
	v_sub_f32_e32 v9, v20, v32
	v_add_f32_e32 v8, v64, v8
	v_exp_f32_e32 v68, v9
	v_sub_f32_e32 v9, v21, v32
	v_add_f32_e32 v8, v65, v8
	v_exp_f32_e32 v69, v9
	v_sub_f32_e32 v9, v22, v32
	v_add_f32_e32 v8, v66, v8
	v_exp_f32_e32 v70, v9
	v_sub_f32_e32 v9, v23, v32
	v_add_f32_e32 v8, v67, v8
	v_exp_f32_e32 v71, v9
	v_sub_f32_e32 v9, v24, v32
	v_add_f32_e32 v8, v68, v8
	v_exp_f32_e32 v72, v9
	v_sub_f32_e32 v9, v25, v32
	v_add_f32_e32 v8, v69, v8
	v_exp_f32_e32 v73, v9
	v_sub_f32_e32 v9, v26, v32
	v_add_f32_e32 v8, v70, v8
	v_exp_f32_e32 v74, v9
	v_sub_f32_e32 v9, v27, v32
	v_add_f32_e32 v8, v71, v8
	v_exp_f32_e32 v75, v9
	v_sub_f32_e32 v9, v28, v32
	v_add_f32_e32 v8, v72, v8
	v_exp_f32_e32 v76, v9
	v_sub_f32_e32 v9, v29, v32
	v_add_f32_e32 v8, v73, v8
	v_exp_f32_e32 v77, v9
	v_sub_f32_e32 v9, v30, v32
	v_add_f32_e32 v8, v74, v8
	v_exp_f32_e32 v78, v9
	v_sub_f32_e32 v9, v31, v32
	v_add_f32_e32 v8, v75, v8
	v_exp_f32_e32 v79, v9
	v_sub_f32_e32 v9, v135, v32
	v_add_f32_e32 v8, v76, v8
	v_exp_f32_e32 v135, v9
	v_sub_f32_e32 v9, v137, v32
	v_add_f32_e32 v8, v77, v8
	v_exp_f32_e32 v137, v9
	v_sub_f32_e32 v9, v113, v32
	v_add_f32_e32 v8, v78, v8
	v_exp_f32_e32 v113, v9
	v_sub_f32_e32 v9, v138, v32
	v_add_f32_e32 v8, v79, v8
	v_exp_f32_e32 v138, v9
	v_sub_f32_e32 v9, v139, v32
	v_add_f32_e32 v8, v135, v8
	v_exp_f32_e32 v139, v9
	v_sub_f32_e32 v9, v158, v32
	v_add_f32_e32 v8, v137, v8
	v_exp_f32_e32 v157, v9
	v_sub_f32_e32 v9, v159, v32
	v_add_f32_e32 v8, v113, v8
	v_exp_f32_e32 v158, v9
	v_sub_f32_e32 v9, v160, v32
	v_add_f32_e32 v8, v138, v8
	v_exp_f32_e32 v159, v9
	v_sub_f32_e32 v9, v161, v32
	v_add_f32_e32 v8, v139, v8
	v_exp_f32_e32 v160, v9
	v_sub_f32_e32 v9, v162, v32
	v_add_f32_e32 v8, v157, v8
	v_exp_f32_e32 v161, v9
	v_sub_f32_e32 v9, v163, v32
	v_add_f32_e32 v8, v158, v8
	v_exp_f32_e32 v162, v9
	v_sub_f32_e32 v9, v164, v32
	v_add_f32_e32 v8, v159, v8
	v_exp_f32_e32 v163, v9
	v_sub_f32_e32 v9, v165, v32
	v_add_f32_e32 v8, v160, v8
	v_exp_f32_e32 v164, v9
	v_sub_f32_e32 v9, v166, v32
	v_add_f32_e32 v8, v161, v8
	v_exp_f32_e32 v165, v9
	v_sub_f32_e32 v9, v167, v32
	v_add_f32_e32 v8, v162, v8
	v_exp_f32_e32 v166, v9
	v_sub_f32_e32 v9, v168, v32
	v_add_f32_e32 v8, v163, v8
	v_exp_f32_e32 v167, v9
	v_sub_f32_e32 v9, v169, v32
	v_add_f32_e32 v8, v164, v8
	v_exp_f32_e32 v168, v9
	v_sub_f32_e32 v9, v170, v32
	v_add_f32_e32 v8, v165, v8
	v_exp_f32_e32 v169, v9
	v_sub_f32_e32 v9, v171, v32
	v_add_f32_e32 v8, v166, v8
	v_exp_f32_e32 v170, v9
	v_sub_f32_e32 v9, v172, v32
	v_add_f32_e32 v8, v167, v8
	v_exp_f32_e32 v171, v9
	v_sub_f32_e32 v9, v52, v32
	v_add_f32_e32 v8, v168, v8
	v_exp_f32_e32 v172, v9
	v_sub_f32_e32 v9, v53, v32
	v_add_f32_e32 v8, v169, v8
	v_exp_f32_e32 v177, v9
	v_sub_f32_e32 v9, v54, v32
	v_add_f32_e32 v8, v170, v8
	v_exp_f32_e32 v178, v9
	v_add3_u32 v9, s36, v146, v145
	v_add_f32_e32 v8, v171, v8
	v_add_u32_e32 v179, 0x6800, v9
	v_add_f32_e32 v8, v172, v8
	v_cvt_pk_bf16_f32 v0, v0, v1
	v_cvt_pk_bf16_f32 v1, v2, v3
	v_cvt_pk_bf16_f32 v2, v4, v5
	v_cvt_pk_bf16_f32 v3, v6, v7
	ds_read2_b64 v[4:7], v179 offset0:128 offset1:130
	v_add_f32_e32 v8, v177, v8
	v_add_f32_e32 v52, v178, v8
	v_sub_f32_e32 v8, v55, v32
	v_exp_f32_e32 v180, v8
	v_sub_f32_e32 v8, v56, v32
	v_add_u32_e32 v182, 0x9800, v9
	v_exp_f32_e32 v181, v8
	ds_read2_b64 v[8:11], v182 offset0:192 offset1:194
	s_waitcnt lgkmcnt(1)
	v_mfma_f32_32x32x16_bf16 v[16:31], v[4:7], v[0:3], 0
	v_add_f32_e32 v4, v180, v52
	v_cvt_pk_bf16_f32 v52, v58, v57
	v_cvt_pk_bf16_f32 v53, v59, v60
	v_sub_f32_e32 v60, v173, v32
	v_cvt_pk_bf16_f32 v54, v12, v13
	v_cvt_pk_bf16_f32 v55, v14, v15
	ds_read2_b64 v[56:59], v179 offset0:132 offset1:134
	v_exp_f32_e32 v173, v60
	v_sub_f32_e32 v60, v174, v32
	v_exp_f32_e32 v174, v60
	v_sub_f32_e32 v60, v175, v32
	v_exp_f32_e32 v175, v60
	ds_read2_b64 v[60:63], v182 offset0:196 offset1:198
	v_add_f32_e32 v183, v181, v4
	s_waitcnt lgkmcnt(2)
	v_mfma_f32_32x32x16_bf16 v[0:15], v[8:11], v[0:3], 0
	v_sub_f32_e32 v51, v51, v32
	v_sub_f32_e32 v50, v50, v32
	v_sub_f32_e32 v48, v48, v32
	v_sub_f32_e32 v45, v45, v32
	v_sub_f32_e32 v44, v44, v32
	v_sub_f32_e32 v43, v43, v32
	v_sub_f32_e32 v42, v42, v32
	s_waitcnt lgkmcnt(1)
	v_mfma_f32_32x32x16_bf16 v[16:31], v[56:59], v[52:55], v[16:31]
	v_sub_f32_e32 v56, v176, v32
	v_exp_f32_e32 v176, v56
	v_cvt_pk_bf16_f32 v56, v64, v65
	v_cvt_pk_bf16_f32 v57, v66, v67
	v_cvt_pk_bf16_f32 v58, v68, v69
	v_cvt_pk_bf16_f32 v59, v70, v71
	ds_read2_b64 v[64:67], v179 offset0:136 offset1:138
	s_waitcnt lgkmcnt(1)
	v_mfma_f32_32x32x16_bf16 v[0:15], v[60:63], v[52:55], v[0:15]
	v_add_f32_e32 v52, v173, v183
	v_add_f32_e32 v52, v174, v52
	v_add_f32_e32 v52, v175, v52
	v_add_f32_e32 v68, v176, v52
	ds_read2_b64 v[52:55], v182 offset0:200 offset1:202
	v_exp_f32_e32 v69, v51
	v_exp_f32_e32 v70, v50
	s_waitcnt lgkmcnt(1)
	v_mfma_f32_32x32x16_bf16 v[16:31], v[64:67], v[56:59], v[16:31]
	v_cvt_pk_bf16_f32 v60, v72, v73
	v_cvt_pk_bf16_f32 v61, v74, v75
	v_cvt_pk_bf16_f32 v62, v76, v77
	v_cvt_pk_bf16_f32 v63, v78, v79
	ds_read2_b64 v[64:67], v179 offset0:140 offset1:142
	v_add_f32_e32 v50, v69, v68
	v_exp_f32_e32 v68, v48
	v_sub_f32_e32 v48, v49, v32
	s_waitcnt lgkmcnt(1)
	v_mfma_f32_32x32x16_bf16 v[0:15], v[52:55], v[56:59], v[0:15]
	v_add_f32_e32 v52, v70, v50
	v_exp_f32_e32 v71, v48
	ds_read2_b64 v[48:51], v182 offset0:204 offset1:206
	v_add_f32_e32 v52, v68, v52
	v_exp_f32_e32 v72, v44
	v_exp_f32_e32 v73, v43
	v_sub_f32_e32 v40, v40, v32
	s_waitcnt lgkmcnt(1)
	v_mfma_f32_32x32x16_bf16 v[16:31], v[64:67], v[60:63], v[16:31]
	v_add_f32_e32 v64, v71, v52
	v_cvt_pk_bf16_f32 v52, v135, v137
	v_cvt_pk_bf16_f32 v53, v113, v138
	v_cvt_pk_bf16_f32 v54, v139, v157
	v_cvt_pk_bf16_f32 v55, v158, v159
	ds_read2_b64 v[56:59], v179 offset0:144 offset1:146
	v_exp_f32_e32 v65, v45
	v_sub_f32_e32 v45, v46, v32
	s_waitcnt lgkmcnt(1)
	v_mfma_f32_32x32x16_bf16 v[0:15], v[48:51], v[60:63], v[0:15]
	v_exp_f32_e32 v66, v45
	v_sub_f32_e32 v45, v47, v32
	ds_read2_b64 v[46:49], v182 offset0:208 offset1:210
	v_exp_f32_e32 v67, v45
	v_add_f32_e32 v44, v65, v64
	v_add_f32_e32 v44, v66, v44
	v_sub_f32_e32 v39, v39, v32
	s_waitcnt lgkmcnt(1)
	v_mfma_f32_32x32x16_bf16 v[16:31], v[56:59], v[52:55], v[16:31]
	v_cvt_pk_bf16_f32 v56, v160, v161
	v_cvt_pk_bf16_f32 v57, v162, v163
	v_cvt_pk_bf16_f32 v58, v164, v165
	v_cvt_pk_bf16_f32 v59, v166, v167
	ds_read2_b64 v[60:63], v179 offset0:148 offset1:150
	v_add_f32_e32 v44, v67, v44
	v_add_f32_e32 v64, v72, v44
	s_waitcnt lgkmcnt(1)
	v_mfma_f32_32x32x16_bf16 v[0:15], v[46:49], v[52:55], v[0:15]
	ds_read2_b64 v[44:47], v182 offset0:212 offset1:214
	v_cvt_pk_bf16_f32 v48, v168, v169
	v_cvt_pk_bf16_f32 v49, v170, v171
	v_cvt_pk_bf16_f32 v50, v172, v177
	v_cvt_pk_bf16_f32 v51, v178, v180
	ds_read2_b64 v[52:55], v179 offset0:152 offset1:154
	v_sub_f32_e32 v38, v38, v32
	s_waitcnt lgkmcnt(2)
	v_mfma_f32_32x32x16_bf16 v[16:31], v[60:63], v[56:59], v[16:31]
	v_exp_f32_e32 v60, v42
	v_add_f32_e32 v42, v73, v64
	v_sub_f32_e32 v34, v34, v32
	v_sub_f32_e32 v37, v37, v32
	v_exp_f32_e32 v61, v37
	v_sub_f32_e32 v33, v33, v32
	v_exp_f32_e32 v33, v33
	s_waitcnt lgkmcnt(1)
	v_mfma_f32_32x32x16_bf16 v[0:15], v[44:47], v[56:59], v[0:15]
	v_exp_f32_e32 v57, v40
	v_sub_f32_e32 v40, v41, v32
	v_add_f32_e32 v56, v60, v42
	v_exp_f32_e32 v58, v40
	ds_read2_b64 v[40:43], v182 offset0:216 offset1:218
	v_exp_f32_e32 v59, v39
	v_cvt_pk_bf16_f32 v44, v181, v173
	s_waitcnt lgkmcnt(0)
	v_mfma_f32_32x32x16_bf16 v[0:15], v[40:43], v[48:51], v[0:15]
	v_exp_f32_e32 v42, v38
	v_add_f32_e32 v38, v57, v56
	v_add_f32_e32 v38, v58, v38
	v_add_f32_e32 v38, v59, v38
	v_cvt_pk_bf16_f32 v45, v174, v175
	v_cvt_pk_bf16_f32 v46, v176, v69
	v_cvt_pk_bf16_f32 v47, v70, v68
	v_mfma_f32_32x32x16_bf16 v[16:31], v[52:55], v[48:51], v[16:31]
	ds_read2_b64 v[52:55], v179 offset0:156 offset1:158
	v_add_f32_e32 v56, v42, v38
	ds_read2_b64 v[38:41], v182 offset0:220 offset1:222
	v_cvt_pk_bf16_f32 v48, v71, v65
	v_cvt_pk_bf16_f32 v49, v66, v67
	v_cvt_pk_bf16_f32 v50, v72, v73
	v_cvt_pk_bf16_f32 v51, v60, v57
	s_waitcnt lgkmcnt(1)
	v_mfma_f32_32x32x16_bf16 v[16:31], v[52:55], v[44:47], v[16:31]
	ds_read2_b64 v[52:55], v179 offset0:160 offset1:162
	s_addc_u32 s3, s21, s3
	s_add_u32 s2, s2, s14
	s_addc_u32 s3, s3, s15
	s_lshl_b32 s6, s8, 6
	s_ashr_i32 s8, s6, 31
	s_add_u32 s2, s2, s6
	s_waitcnt lgkmcnt(1)
	v_mfma_f32_32x32x16_bf16 v[0:15], v[38:41], v[44:47], v[0:15]
	v_exp_f32_e32 v46, v34
	v_sub_f32_e32 v34, v35, v32
	v_exp_f32_e32 v47, v34
	v_sub_f32_e32 v34, v36, v32
	v_exp_f32_e32 v57, v34
	ds_read2_b64 v[34:37], v182 offset0:224 offset1:226
	v_cvt_pk_bf16_f32 v38, v58, v59
	v_cvt_pk_bf16_f32 v39, v42, v61
	v_cvt_pk_bf16_f32 v40, v46, v47
	v_cvt_pk_bf16_f32 v41, v57, v33
	ds_read2_b64 v[42:45], v179 offset0:164 offset1:166
	s_waitcnt lgkmcnt(2)
	v_mfma_f32_32x32x16_bf16 v[16:31], v[52:55], v[48:51], v[16:31]
	s_addc_u32 s3, s3, s8
	s_andn2_b64 vcc, exec, s[12:13]
	s_xor_b32 s34, s34, 1
	s_waitcnt lgkmcnt(1)
	v_mfma_f32_32x32x16_bf16 v[0:15], v[34:37], v[48:51], v[0:15]
	v_add_f32_e32 v34, v61, v56
	v_add_f32_e32 v34, v46, v34
	v_add_f32_e32 v34, v47, v34
	v_add_f32_e32 v34, v57, v34
	v_add_f32_e32 v36, v33, v34
	ds_bpermute_b32 v37, v141, v36
	v_fma_f32 v46, v156, s31, -v32
	s_waitcnt lgkmcnt(1)
	v_mfma_f32_32x32x16_bf16 v[16:31], v[42:45], v[38:41], v[16:31]
	ds_read2_b64 v[32:35], v182 offset0:228 offset1:230
	v_exp_f32_e32 v42, v46
	s_waitcnt lgkmcnt(1)
	v_add_f32_e32 v36, v36, v37
	v_add_f32_e32 v36, v42, v36
	v_rcp_f32_e32 v36, v36
	s_waitcnt lgkmcnt(0)
	v_mfma_f32_32x32x16_bf16 v[0:15], v[32:35], v[38:41], v[0:15]
	v_mul_f32_e32 v32, 0x41000000, v36
	s_nop 2
	v_mul_f32_e32 v16, v32, v16
	v_mul_f32_e32 v17, v32, v17
	v_mov_b32_e32 v33, v112
	v_cvt_pk_fp8_f32 v33, v16, v17
	v_mul_f32_e32 v16, v32, v20
	v_mul_f32_e32 v17, v32, v21
	v_mov_b32_e32 v20, v112
	v_cvt_pk_fp8_f32 v20, v16, v17
	v_mul_f32_e32 v16, v32, v22
	v_mul_f32_e32 v17, v32, v23
	v_mov_b32_e32 v21, v112
	v_cvt_pk_fp8_f32 v20, v16, v17 op_sel:[0,0,1]
	v_mul_f32_e32 v16, v32, v24
	v_mul_f32_e32 v17, v32, v25
	v_cvt_pk_fp8_f32 v21, v16, v17
	v_mul_f32_e32 v16, v32, v28
	v_mul_f32_e32 v17, v32, v29
	v_mov_b32_e32 v22, v112
	v_cvt_pk_fp8_f32 v22, v16, v17
	v_mul_f32_e32 v16, v32, v30
	v_mul_f32_e32 v17, v32, v31
	v_mul_f32_e32 v0, v32, v0
	v_cvt_pk_fp8_f32 v22, v16, v17 op_sel:[0,0,1]
	v_mul_f32_e32 v1, v32, v1
	v_mov_b32_e32 v16, v112
	v_cvt_pk_fp8_f32 v16, v0, v1
	v_mul_f32_e32 v0, v32, v4
	v_mul_f32_e32 v1, v32, v5
	v_mov_b32_e32 v4, v112
	v_cvt_pk_fp8_f32 v4, v0, v1
	v_mul_f32_e32 v0, v32, v6
	v_mul_f32_e32 v1, v32, v7
	v_mov_b32_e32 v5, v112
	v_cvt_pk_fp8_f32 v4, v0, v1 op_sel:[0,0,1]
	v_mul_f32_e32 v0, v32, v8
	v_mul_f32_e32 v1, v32, v9
	v_cvt_pk_fp8_f32 v5, v0, v1
	v_mul_f32_e32 v0, v32, v12
	v_mul_f32_e32 v1, v32, v13
	v_mov_b32_e32 v6, v112
	v_mul_f32_e32 v18, v32, v18
	v_mul_f32_e32 v19, v32, v19
	v_cvt_pk_fp8_f32 v6, v0, v1
	v_cvt_pk_fp8_f32 v33, v18, v19 op_sel:[0,0,1]
	v_mul_f32_e32 v18, v32, v26
	v_mul_f32_e32 v19, v32, v27
	v_cvt_pk_fp8_f32 v21, v18, v19 op_sel:[0,0,1]
	v_mul_f32_e32 v2, v32, v2
	v_mul_f32_e32 v3, v32, v3
	v_cvt_pk_fp8_f32 v16, v2, v3 op_sel:[0,0,1]
	v_mul_f32_e32 v2, v32, v10
	v_mul_f32_e32 v3, v32, v11
	v_mul_f32_e32 v0, v32, v14
	v_mul_f32_e32 v1, v32, v15
	v_cvt_pk_fp8_f32 v5, v2, v3 op_sel:[0,0,1]
	v_cvt_pk_fp8_f32 v6, v0, v1 op_sel:[0,0,1]
	ds_write2_b32 v153, v33, v20 offset1:2
	ds_write2_b32 v153, v21, v22 offset0:4 offset1:6
	ds_write2_b32 v153, v16, v4 offset0:8 offset1:10
	ds_write2_b32 v153, v5, v6 offset0:12 offset1:14
	s_waitcnt lgkmcnt(0)
	ds_read_b128 v[0:3], v154
	ds_read_b128 v[4:7], v154 offset:2304
	v_lshl_add_u64 v[8:9], s[2:3], 0, v[128:129]
	v_lshl_add_u64 v[10:11], v[8:9], 0, v[130:131]
	s_waitcnt lgkmcnt(1)
	global_store_dwordx4 v[10:11], v[0:3], off
	s_nop 1
	v_lshl_add_u64 v[0:1], v[8:9], 0, v[132:133]
	s_waitcnt lgkmcnt(0)
	global_store_dwordx4 v[0:1], v[4:7], off
	s_cbranch_vccnz .LBB0_868
	s_mul_i32 s2, s34, 0xd000
	s_add_i32 s2, s2, 0
	v_add_u32_e32 v0, s2, v142
	v_add_u32_e32 v2, v0, v147
	v_add_u32_e32 v1, v0, v143
	s_waitcnt vmcnt(6)
	ds_write_b128 v2, v[80:83]
	ds_write_b128 v1, v[84:87] offset:27648
	v_add_u32_e32 v2, v0, v148
	v_add_u32_e32 v0, v0, v149
	ds_write_b128 v2, v[88:91]
	ds_write_b128 v1, v[108:111] offset:27776
	ds_write_b128 v0, v[114:117]
	ds_write_b128 v1, v[118:121] offset:27904
	s_branch .LBB0_868
